# speedup vs baseline: 1.0052x; 1.0009x over previous
.Lu0_1:
	ds_read_b64_tr_b16 v[178:179], v206 offset:24576
	ds_read_b64_tr_b16 v[180:181], v206 offset:25600
	s_waitcnt lgkmcnt(9)
	v_mfma_f32_32x32x16_f16 v[98:113], v[82:85], v[154:157], v[34:49]
	v_add_f32_e32 v86, v66, v67
	v_add_f32_e32 v86, v68, v86
	v_add_f32_e32 v86, v69, v86
	v_add_f32_e32 v86, v70, v86
	v_add_f32_e32 v86, v71, v86
	v_cvt_pk_f16_f32 v158, v66, v67
	v_cvt_pk_f16_f32 v159, v68, v69
	ds_read_b64_tr_b16 v[174:175], v207 offset:24576
	ds_read_b64_tr_b16 v[176:177], v207 offset:25600
	v_add_f32_e32 v66, v72, v86
	s_waitcnt lgkmcnt(10)
	v_mfma_f32_32x32x16_f16 v[82:97], v[170:173], v[154:157], v[34:49]
	v_add_f32_e32 v66, v73, v66
	v_add_f32_e32 v66, v74, v66
	v_add_f32_e32 v66, v75, v66
	v_cvt_pk_f16_f32 v160, v70, v71
	v_cvt_pk_f16_f32 v161, v72, v73
	ds_read_b64_tr_b16 v[170:171], v206 offset:26624
	ds_read_b64_tr_b16 v[172:173], v206 offset:27648
	s_waitcnt lgkmcnt(11)
	v_mfma_f32_32x32x16_f16 v[98:113], v[166:169], v[146:149], v[98:113]
	v_add_f32_e32 v66, v76, v66
	v_add_f32_e32 v66, v77, v66
	v_add_f32_e32 v66, v78, v66
	v_add_f32_e32 v66, v79, v66
	v_cvt_pk_f16_f32 v150, v74, v75
	v_cvt_pk_f16_f32 v151, v76, v77
	ds_read_b64_tr_b16 v[74:75], v207 offset:26624
	ds_read_b64_tr_b16 v[76:77], v207 offset:27648
	s_waitcnt lgkmcnt(12)
	v_mfma_f32_32x32x16_f16 v[82:97], v[162:165], v[146:149], v[82:97]
	v_add_f32_e32 v66, v80, v66
	v_add_f32_e32 v66, v81, v66
	v_add_f32_e32 v66, v50, v66
	v_add_f32_e32 v66, v51, v66
	v_cvt_pk_f16_f32 v152, v78, v79
	v_cvt_pk_f16_f32 v153, v80, v81
	ds_read_b64_tr_b16 v[70:71], v206 offset:28672
	ds_read_b64_tr_b16 v[72:73], v206 offset:29696
	s_waitcnt lgkmcnt(13)
	v_mfma_f32_32x32x16_f16 v[98:113], v[126:129], v[138:141], v[98:113]
	v_add_f32_e32 v66, v52, v66
	v_add_f32_e32 v66, v53, v66
	v_add_f32_e32 v66, v54, v66
	v_add_f32_e32 v78, v55, v66
	v_cvt_pk_f16_f32 v142, v50, v51
	v_cvt_pk_f16_f32 v143, v52, v53
	ds_read_b64_tr_b16 v[66:67], v207 offset:28672
	ds_read_b64_tr_b16 v[68:69], v207 offset:29696
	s_waitcnt lgkmcnt(14)
	v_mfma_f32_32x32x16_f16 v[82:97], v[122:125], v[138:141], v[82:97]
	v_add_f32_e32 v50, v56, v78
	v_add_f32_e32 v50, v57, v50
	v_add_f32_e32 v50, v58, v50
	v_add_f32_e32 v50, v59, v50
	v_cvt_pk_f16_f32 v144, v54, v55
	v_cvt_pk_f16_f32 v145, v56, v57
	ds_read_b64_tr_b16 v[54:55], v206 offset:30720
	ds_read_b64_tr_b16 v[56:57], v206 offset:31744
	s_waitcnt lgkmcnt(14)
	v_mfma_f32_32x32x16_f16 v[98:113], v[118:121], v[134:137], v[98:113]
	v_add_f32_e32 v50, v60, v50
	v_add_f32_e32 v50, v61, v50
	v_add_f32_e32 v50, v62, v50
	v_add_f32_e32 v78, v63, v50
	v_cvt_pk_f16_f32 v130, v58, v59
	v_cvt_pk_f16_f32 v131, v60, v61
	ds_read_b64_tr_b16 v[50:51], v207 offset:30720
	ds_read_b64_tr_b16 v[52:53], v207 offset:31744
	v_mfma_f32_32x32x16_f16 v[82:97], v[114:117], v[134:137], v[82:97]
	v_add_f32_e32 v58, v64, v78
	v_add_f32_e32 v60, v65, v58
	v_cvt_pk_f16_f32 v132, v62, v63
	v_cvt_pk_f16_f32 v133, v64, v65
	s_add_i32 s26, s42, s36
	s_mov_b32 m0, s26
	s_nop 0
	global_load_lds_dwordx4 v221, s[50:51]
	s_add_i32 s26, s39, s35
	s_mov_b32 m0, s26
	s_nop 0
	global_load_lds_dwordx4 v222, s[52:53]
	v_max_f32_e32 v58, v98, v99
	v_max3_f32 v59, v100, v101, v83
	v_max3_f32 v58, v58, v82, v84
	v_max3_f32 v58, v58, v85, v102
	v_max3_f32 v59, v59, v104, v105
	v_max3_f32 v58, v58, v103, v86
	v_max3_f32 v59, v59, v88, v89
	v_max3_f32 v58, v58, v87, v106
	v_max3_f32 v59, v59, v108, v109
	v_max3_f32 v58, v58, v107, v90
	v_max3_f32 v59, v59, v92, v93
	v_max3_f32 v58, v58, v91, v110
	v_max3_f32 v59, v59, v112, v113
	v_max3_f32 v58, v58, v111, v94
	v_max3_f32 v59, v59, v96, v97
	v_max3_f32 v58, v58, v95, v59
	v_add_f32_e32 v198, v183, v60
	v_cmp_lt_f32_e32 vcc, s41, v58
	s_cmp_lg_u64 vcc, 0
	s_cselect_b64 s[26:27], -1, 0
	s_cbranch_vccnz .Lu0_9

.Lu0_4:
	s_add_i32 s26, s39, 0x2000
	s_cmpk_lg_i32 s39, 0x4000
	s_cselect_b32 s43, s26, 0
	ds_read_b64_tr_b16 v[126:127], v206 offset:32768
	ds_read_b64_tr_b16 v[128:129], v206 offset:33792
	s_waitcnt lgkmcnt(9)
	v_mfma_f32_32x32x16_f16 v[66:81], v[58:61], v[154:157], v[34:49]
	v_add_f32_e32 v50, v98, v99
	v_add_f32_e32 v50, v100, v50
	v_add_f32_e32 v50, v101, v50
	v_add_f32_e32 v50, v102, v50
	v_add_f32_e32 v50, v103, v50
	v_cvt_pk_f16_f32 v158, v98, v99
	v_cvt_pk_f16_f32 v159, v100, v101
	ds_read_b64_tr_b16 v[122:123], v207 offset:32768
	ds_read_b64_tr_b16 v[124:125], v207 offset:33792
	v_add_f32_e32 v50, v104, v50
	v_add_f32_e32 v50, v105, v50
	v_add_f32_e32 v50, v106, v50
	v_add_f32_e32 v98, v107, v50
	s_waitcnt lgkmcnt(10)
	v_mfma_f32_32x32x16_f16 v[50:65], v[114:117], v[154:157], v[34:49]
	v_cvt_pk_f16_f32 v160, v102, v103
	v_cvt_pk_f16_f32 v161, v104, v105
	ds_read_b64_tr_b16 v[118:119], v206 offset:34816
	ds_read_b64_tr_b16 v[120:121], v206 offset:35840
	s_waitcnt lgkmcnt(11)
	v_mfma_f32_32x32x16_f16 v[66:81], v[182:185], v[146:149], v[66:81]
	v_add_f32_e32 v98, v108, v98
	v_add_f32_e32 v98, v109, v98
	v_add_f32_e32 v98, v110, v98
	v_add_f32_e32 v98, v111, v98
	v_cvt_pk_f16_f32 v150, v106, v107
	v_cvt_pk_f16_f32 v151, v108, v109
	ds_read_b64_tr_b16 v[114:115], v207 offset:34816
	ds_read_b64_tr_b16 v[116:117], v207 offset:35840
	s_waitcnt lgkmcnt(12)
	v_mfma_f32_32x32x16_f16 v[50:65], v[174:177], v[146:149], v[50:65]
	v_add_f32_e32 v98, v112, v98
	v_add_f32_e32 v98, v113, v98
	v_add_f32_e32 v98, v82, v98
	v_add_f32_e32 v98, v83, v98
	v_cvt_pk_f16_f32 v152, v110, v111
	v_cvt_pk_f16_f32 v153, v112, v113
	ds_read_b64_tr_b16 v[106:107], v206 offset:36864
	ds_read_b64_tr_b16 v[108:109], v206 offset:37888
	s_waitcnt lgkmcnt(13)
	v_mfma_f32_32x32x16_f16 v[66:81], v[178:181], v[138:141], v[66:81]
	v_add_f32_e32 v98, v84, v98
	v_add_f32_e32 v98, v85, v98
	v_add_f32_e32 v98, v86, v98
	v_add_f32_e32 v98, v87, v98
	v_cvt_pk_f16_f32 v142, v82, v83
	v_cvt_pk_f16_f32 v143, v84, v85
	ds_read_b64_tr_b16 v[102:103], v207 offset:36864
	ds_read_b64_tr_b16 v[104:105], v207 offset:37888
	s_waitcnt lgkmcnt(14)
	v_mfma_f32_32x32x16_f16 v[50:65], v[166:169], v[138:141], v[50:65]
	v_add_f32_e32 v82, v88, v98
	v_add_f32_e32 v82, v89, v82
	v_add_f32_e32 v82, v90, v82
	v_add_f32_e32 v82, v91, v82
	v_cvt_pk_f16_f32 v144, v86, v87
	v_cvt_pk_f16_f32 v145, v88, v89
	ds_read_b64_tr_b16 v[98:99], v206 offset:38912
	ds_read_b64_tr_b16 v[100:101], v206 offset:39936
	s_waitcnt lgkmcnt(14)
	v_mfma_f32_32x32x16_f16 v[66:81], v[170:173], v[134:137], v[66:81]
	v_add_f32_e32 v82, v92, v82
	v_add_f32_e32 v82, v93, v82
	v_add_f32_e32 v82, v94, v82
	v_add_f32_e32 v82, v95, v82
	v_cvt_pk_f16_f32 v130, v90, v91
	v_cvt_pk_f16_f32 v131, v92, v93
	ds_read_b64_tr_b16 v[86:87], v207 offset:38912
	ds_read_b64_tr_b16 v[88:89], v207 offset:39936
	v_mfma_f32_32x32x16_f16 v[50:65], v[162:165], v[134:137], v[50:65]
	v_add_f32_e32 v82, v96, v82
	v_add_f32_e32 v84, v97, v82
	v_cvt_pk_f16_f32 v132, v94, v95
	v_cvt_pk_f16_f32 v133, v96, v97
	s_add_u32 s54, s50, 0x2000
	s_addc_u32 s55, s51, 0
	s_add_i32 s26, s39, s36
	s_mov_b32 m0, s26
	s_nop 0
	global_load_lds_dwordx4 v221, s[54:55]
	v_max_f32_e32 v82, v66, v67
	s_nop 1
	v_max3_f32 v83, v68, v69, v51
	v_max3_f32 v82, v82, v50, v52
	v_max3_f32 v82, v82, v53, v70
	v_max3_f32 v83, v83, v72, v73
	v_max3_f32 v82, v82, v71, v54
	v_max3_f32 v83, v83, v56, v57
	v_max3_f32 v82, v82, v55, v74
	v_max3_f32 v83, v83, v76, v77
	v_max3_f32 v82, v82, v75, v58
	v_max3_f32 v83, v83, v60, v61
	v_max3_f32 v82, v82, v59, v78
	v_max3_f32 v83, v83, v80, v81
	v_max3_f32 v82, v82, v79, v62
	v_max3_f32 v83, v83, v64, v65
	v_max3_f32 v82, v82, v63, v83
	v_add_f32_e32 v183, v198, v84
	s_add_u32 s54, s52, 0x2000
	s_addc_u32 s55, s53, 0
	s_add_i32 s26, s43, s35
	s_mov_b32 m0, s26
	s_nop 0
	global_load_lds_dwordx4 v222, s[54:55]
	v_cmp_lt_f32_e32 vcc, s41, v82
	s_cmp_lg_u64 vcc, 0
	s_cselect_b64 s[26:27], -1, 0
	s_cbranch_vccnz .Lu0_12

.Lu1_1:
	ds_read_b64_tr_b16 v[178:179], v206 offset:40960
	ds_read_b64_tr_b16 v[180:181], v206 offset:41984
	s_waitcnt lgkmcnt(9)
	v_mfma_f32_32x32x16_f16 v[98:113], v[82:85], v[154:157], v[34:49]
	v_add_f32_e32 v86, v66, v67
	v_add_f32_e32 v86, v68, v86
	v_add_f32_e32 v86, v69, v86
	v_add_f32_e32 v86, v70, v86
	v_add_f32_e32 v86, v71, v86
	v_cvt_pk_f16_f32 v158, v66, v67
	v_cvt_pk_f16_f32 v159, v68, v69
	ds_read_b64_tr_b16 v[174:175], v207 offset:40960
	ds_read_b64_tr_b16 v[176:177], v207 offset:41984
	v_add_f32_e32 v66, v72, v86
	s_waitcnt lgkmcnt(10)
	v_mfma_f32_32x32x16_f16 v[82:97], v[170:173], v[154:157], v[34:49]
	v_add_f32_e32 v66, v73, v66
	v_add_f32_e32 v66, v74, v66
	v_add_f32_e32 v66, v75, v66
	v_cvt_pk_f16_f32 v160, v70, v71
	v_cvt_pk_f16_f32 v161, v72, v73
	ds_read_b64_tr_b16 v[170:171], v206 offset:43008
	ds_read_b64_tr_b16 v[172:173], v206 offset:44032
	s_waitcnt lgkmcnt(11)
	v_mfma_f32_32x32x16_f16 v[98:113], v[166:169], v[146:149], v[98:113]
	v_add_f32_e32 v66, v76, v66
	v_add_f32_e32 v66, v77, v66
	v_add_f32_e32 v66, v78, v66
	v_add_f32_e32 v66, v79, v66
	v_cvt_pk_f16_f32 v150, v74, v75
	v_cvt_pk_f16_f32 v151, v76, v77
	ds_read_b64_tr_b16 v[74:75], v207 offset:43008
	ds_read_b64_tr_b16 v[76:77], v207 offset:44032
	s_waitcnt lgkmcnt(12)
	v_mfma_f32_32x32x16_f16 v[82:97], v[162:165], v[146:149], v[82:97]
	v_add_f32_e32 v66, v80, v66
	v_add_f32_e32 v66, v81, v66
	v_add_f32_e32 v66, v50, v66
	v_add_f32_e32 v66, v51, v66
	v_cvt_pk_f16_f32 v152, v78, v79
	v_cvt_pk_f16_f32 v153, v80, v81
	ds_read_b64_tr_b16 v[70:71], v206 offset:45056
	ds_read_b64_tr_b16 v[72:73], v206 offset:46080
	s_waitcnt lgkmcnt(13)
	v_mfma_f32_32x32x16_f16 v[98:113], v[126:129], v[138:141], v[98:113]
	v_add_f32_e32 v66, v52, v66
	v_add_f32_e32 v66, v53, v66
	v_add_f32_e32 v66, v54, v66
	v_add_f32_e32 v78, v55, v66
	v_cvt_pk_f16_f32 v142, v50, v51
	v_cvt_pk_f16_f32 v143, v52, v53
	ds_read_b64_tr_b16 v[66:67], v207 offset:45056
	ds_read_b64_tr_b16 v[68:69], v207 offset:46080
	s_waitcnt lgkmcnt(14)
	v_mfma_f32_32x32x16_f16 v[82:97], v[122:125], v[138:141], v[82:97]
	v_add_f32_e32 v50, v56, v78
	v_add_f32_e32 v50, v57, v50
	v_add_f32_e32 v50, v58, v50
	v_add_f32_e32 v50, v59, v50
	v_cvt_pk_f16_f32 v144, v54, v55
	v_cvt_pk_f16_f32 v145, v56, v57
	ds_read_b64_tr_b16 v[54:55], v206 offset:47104
	ds_read_b64_tr_b16 v[56:57], v206 offset:48128
	s_waitcnt lgkmcnt(14)
	v_mfma_f32_32x32x16_f16 v[98:113], v[118:121], v[134:137], v[98:113]
	v_add_f32_e32 v50, v60, v50
	v_add_f32_e32 v50, v61, v50
	v_add_f32_e32 v50, v62, v50
	v_add_f32_e32 v78, v63, v50
	v_cvt_pk_f16_f32 v130, v58, v59
	v_cvt_pk_f16_f32 v131, v60, v61
	ds_read_b64_tr_b16 v[50:51], v207 offset:47104
	ds_read_b64_tr_b16 v[52:53], v207 offset:48128
	v_mfma_f32_32x32x16_f16 v[82:97], v[114:117], v[134:137], v[82:97]
	v_add_f32_e32 v58, v64, v78
	v_add_f32_e32 v60, v65, v58
	v_cvt_pk_f16_f32 v132, v62, v63
	v_cvt_pk_f16_f32 v133, v64, v65
	s_add_i32 s26, s42, s36
	s_mov_b32 m0, s26
	s_nop 0
	global_load_lds_dwordx4 v221, s[50:51]
	s_add_i32 s26, s39, s35
	s_mov_b32 m0, s26
	s_nop 0
	global_load_lds_dwordx4 v222, s[52:53]
	v_max_f32_e32 v58, v98, v99
	v_max3_f32 v59, v100, v101, v83
	v_max3_f32 v58, v58, v82, v84
	v_max3_f32 v58, v58, v85, v102
	v_max3_f32 v59, v59, v104, v105
	v_max3_f32 v58, v58, v103, v86
	v_max3_f32 v59, v59, v88, v89
	v_max3_f32 v58, v58, v87, v106
	v_max3_f32 v59, v59, v108, v109
	v_max3_f32 v58, v58, v107, v90
	v_max3_f32 v59, v59, v92, v93
	v_max3_f32 v58, v58, v91, v110
	v_max3_f32 v59, v59, v112, v113
	v_max3_f32 v58, v58, v111, v94
	v_max3_f32 v59, v59, v96, v97
	v_max3_f32 v58, v58, v95, v59
	v_add_f32_e32 v198, v183, v60
	v_cmp_lt_f32_e32 vcc, s41, v58
	s_cmp_lg_u64 vcc, 0
	s_cselect_b64 s[26:27], -1, 0
	s_cbranch_vccnz .Lu1_9

.Lu1_4:
	s_add_i32 s26, s39, 0x2000
	s_cmpk_lg_i32 s39, 0x4000
	s_cselect_b32 s43, s26, 0
	ds_read_b64_tr_b16 v[126:127], v206 offset:24576
	ds_read_b64_tr_b16 v[128:129], v206 offset:25600
	s_waitcnt lgkmcnt(9)
	v_mfma_f32_32x32x16_f16 v[66:81], v[58:61], v[154:157], v[34:49]
	v_add_f32_e32 v50, v98, v99
	v_add_f32_e32 v50, v100, v50
	v_add_f32_e32 v50, v101, v50
	v_add_f32_e32 v50, v102, v50
	v_add_f32_e32 v50, v103, v50
	v_cvt_pk_f16_f32 v158, v98, v99
	v_cvt_pk_f16_f32 v159, v100, v101
	ds_read_b64_tr_b16 v[122:123], v207 offset:24576
	ds_read_b64_tr_b16 v[124:125], v207 offset:25600
	v_add_f32_e32 v50, v104, v50
	v_add_f32_e32 v50, v105, v50
	v_add_f32_e32 v50, v106, v50
	v_add_f32_e32 v98, v107, v50
	s_waitcnt lgkmcnt(10)
	v_mfma_f32_32x32x16_f16 v[50:65], v[114:117], v[154:157], v[34:49]
	v_cvt_pk_f16_f32 v160, v102, v103
	v_cvt_pk_f16_f32 v161, v104, v105
	ds_read_b64_tr_b16 v[118:119], v206 offset:26624
	ds_read_b64_tr_b16 v[120:121], v206 offset:27648
	s_waitcnt lgkmcnt(11)
	v_mfma_f32_32x32x16_f16 v[66:81], v[182:185], v[146:149], v[66:81]
	v_add_f32_e32 v98, v108, v98
	v_add_f32_e32 v98, v109, v98
	v_add_f32_e32 v98, v110, v98
	v_add_f32_e32 v98, v111, v98
	v_cvt_pk_f16_f32 v150, v106, v107
	v_cvt_pk_f16_f32 v151, v108, v109
	ds_read_b64_tr_b16 v[114:115], v207 offset:26624
	ds_read_b64_tr_b16 v[116:117], v207 offset:27648
	s_waitcnt lgkmcnt(12)
	v_mfma_f32_32x32x16_f16 v[50:65], v[174:177], v[146:149], v[50:65]
	v_add_f32_e32 v98, v112, v98
	v_add_f32_e32 v98, v113, v98
	v_add_f32_e32 v98, v82, v98
	v_add_f32_e32 v98, v83, v98
	v_cvt_pk_f16_f32 v152, v110, v111
	v_cvt_pk_f16_f32 v153, v112, v113
	ds_read_b64_tr_b16 v[106:107], v206 offset:28672
	ds_read_b64_tr_b16 v[108:109], v206 offset:29696
	s_waitcnt lgkmcnt(13)
	v_mfma_f32_32x32x16_f16 v[66:81], v[178:181], v[138:141], v[66:81]
	v_add_f32_e32 v98, v84, v98
	v_add_f32_e32 v98, v85, v98
	v_add_f32_e32 v98, v86, v98
	v_add_f32_e32 v98, v87, v98
	v_cvt_pk_f16_f32 v142, v82, v83
	v_cvt_pk_f16_f32 v143, v84, v85
	ds_read_b64_tr_b16 v[102:103], v207 offset:28672
	ds_read_b64_tr_b16 v[104:105], v207 offset:29696
	s_waitcnt lgkmcnt(14)
	v_mfma_f32_32x32x16_f16 v[50:65], v[166:169], v[138:141], v[50:65]
	v_add_f32_e32 v82, v88, v98
	v_add_f32_e32 v82, v89, v82
	v_add_f32_e32 v82, v90, v82
	v_add_f32_e32 v82, v91, v82
	v_cvt_pk_f16_f32 v144, v86, v87
	v_cvt_pk_f16_f32 v145, v88, v89
	ds_read_b64_tr_b16 v[98:99], v206 offset:30720
	ds_read_b64_tr_b16 v[100:101], v206 offset:31744
	s_waitcnt lgkmcnt(14)
	v_mfma_f32_32x32x16_f16 v[66:81], v[170:173], v[134:137], v[66:81]
	v_add_f32_e32 v82, v92, v82
	v_add_f32_e32 v82, v93, v82
	v_add_f32_e32 v82, v94, v82
	v_add_f32_e32 v82, v95, v82
	v_cvt_pk_f16_f32 v130, v90, v91
	v_cvt_pk_f16_f32 v131, v92, v93
	ds_read_b64_tr_b16 v[86:87], v207 offset:30720
	ds_read_b64_tr_b16 v[88:89], v207 offset:31744
	v_mfma_f32_32x32x16_f16 v[50:65], v[162:165], v[134:137], v[50:65]
	v_add_f32_e32 v82, v96, v82
	v_add_f32_e32 v84, v97, v82
	v_cvt_pk_f16_f32 v132, v94, v95
	v_cvt_pk_f16_f32 v133, v96, v97
	s_add_u32 s54, s50, 0x2000
	s_addc_u32 s55, s51, 0
	s_add_i32 s26, s39, s36
	s_mov_b32 m0, s26
	s_nop 0
	global_load_lds_dwordx4 v221, s[54:55]
	v_max_f32_e32 v82, v66, v67
	s_nop 1
	v_max3_f32 v83, v68, v69, v51
	v_max3_f32 v82, v82, v50, v52
	v_max3_f32 v82, v82, v53, v70
	v_max3_f32 v83, v83, v72, v73
	v_max3_f32 v82, v82, v71, v54
	v_max3_f32 v83, v83, v56, v57
	v_max3_f32 v82, v82, v55, v74
	v_max3_f32 v83, v83, v76, v77
	v_max3_f32 v82, v82, v75, v58
	v_max3_f32 v83, v83, v60, v61
	v_max3_f32 v82, v82, v59, v78
	v_max3_f32 v83, v83, v80, v81
	v_max3_f32 v82, v82, v79, v62
	v_max3_f32 v83, v83, v64, v65
	v_max3_f32 v82, v82, v63, v83
	v_add_f32_e32 v183, v198, v84
	s_add_u32 s54, s52, 0x2000
	s_addc_u32 s55, s53, 0
	s_add_i32 s26, s43, s35
	s_mov_b32 m0, s26
	s_nop 0
	global_load_lds_dwordx4 v222, s[54:55]
	v_cmp_lt_f32_e32 vcc, s41, v82
	s_cmp_lg_u64 vcc, 0
	s_cselect_b64 s[26:27], -1, 0
	s_cbranch_vccnz .Lu1_12

.Lu2_1:
	ds_read_b64_tr_b16 v[178:179], v206 offset:32768
	ds_read_b64_tr_b16 v[180:181], v206 offset:33792
	s_waitcnt lgkmcnt(9)
	v_mfma_f32_32x32x16_f16 v[98:113], v[82:85], v[154:157], v[34:49]
	v_add_f32_e32 v86, v66, v67
	v_add_f32_e32 v86, v68, v86
	v_add_f32_e32 v86, v69, v86
	v_add_f32_e32 v86, v70, v86
	v_add_f32_e32 v86, v71, v86
	v_cvt_pk_f16_f32 v158, v66, v67
	v_cvt_pk_f16_f32 v159, v68, v69
	ds_read_b64_tr_b16 v[174:175], v207 offset:32768
	ds_read_b64_tr_b16 v[176:177], v207 offset:33792
	v_add_f32_e32 v66, v72, v86
	s_waitcnt lgkmcnt(10)
	v_mfma_f32_32x32x16_f16 v[82:97], v[170:173], v[154:157], v[34:49]
	v_add_f32_e32 v66, v73, v66
	v_add_f32_e32 v66, v74, v66
	v_add_f32_e32 v66, v75, v66
	v_cvt_pk_f16_f32 v160, v70, v71
	v_cvt_pk_f16_f32 v161, v72, v73
	ds_read_b64_tr_b16 v[170:171], v206 offset:34816
	ds_read_b64_tr_b16 v[172:173], v206 offset:35840
	s_waitcnt lgkmcnt(11)
	v_mfma_f32_32x32x16_f16 v[98:113], v[166:169], v[146:149], v[98:113]
	v_add_f32_e32 v66, v76, v66
	v_add_f32_e32 v66, v77, v66
	v_add_f32_e32 v66, v78, v66
	v_add_f32_e32 v66, v79, v66
	v_cvt_pk_f16_f32 v150, v74, v75
	v_cvt_pk_f16_f32 v151, v76, v77
	ds_read_b64_tr_b16 v[74:75], v207 offset:34816
	ds_read_b64_tr_b16 v[76:77], v207 offset:35840
	s_waitcnt lgkmcnt(12)
	v_mfma_f32_32x32x16_f16 v[82:97], v[162:165], v[146:149], v[82:97]
	v_add_f32_e32 v66, v80, v66
	v_add_f32_e32 v66, v81, v66
	v_add_f32_e32 v66, v50, v66
	v_add_f32_e32 v66, v51, v66
	v_cvt_pk_f16_f32 v152, v78, v79
	v_cvt_pk_f16_f32 v153, v80, v81
	ds_read_b64_tr_b16 v[70:71], v206 offset:36864
	ds_read_b64_tr_b16 v[72:73], v206 offset:37888
	s_waitcnt lgkmcnt(13)
	v_mfma_f32_32x32x16_f16 v[98:113], v[126:129], v[138:141], v[98:113]
	v_add_f32_e32 v66, v52, v66
	v_add_f32_e32 v66, v53, v66
	v_add_f32_e32 v66, v54, v66
	v_add_f32_e32 v78, v55, v66
	v_cvt_pk_f16_f32 v142, v50, v51
	v_cvt_pk_f16_f32 v143, v52, v53
	ds_read_b64_tr_b16 v[66:67], v207 offset:36864
	ds_read_b64_tr_b16 v[68:69], v207 offset:37888
	s_waitcnt lgkmcnt(14)
	v_mfma_f32_32x32x16_f16 v[82:97], v[122:125], v[138:141], v[82:97]
	v_add_f32_e32 v50, v56, v78
	v_add_f32_e32 v50, v57, v50
	v_add_f32_e32 v50, v58, v50
	v_add_f32_e32 v50, v59, v50
	v_cvt_pk_f16_f32 v144, v54, v55
	v_cvt_pk_f16_f32 v145, v56, v57
	ds_read_b64_tr_b16 v[54:55], v206 offset:38912
	ds_read_b64_tr_b16 v[56:57], v206 offset:39936
	s_waitcnt lgkmcnt(14)
	v_mfma_f32_32x32x16_f16 v[98:113], v[118:121], v[134:137], v[98:113]
	v_add_f32_e32 v50, v60, v50
	v_add_f32_e32 v50, v61, v50
	v_add_f32_e32 v50, v62, v50
	v_add_f32_e32 v78, v63, v50
	v_cvt_pk_f16_f32 v130, v58, v59
	v_cvt_pk_f16_f32 v131, v60, v61
	ds_read_b64_tr_b16 v[50:51], v207 offset:38912
	ds_read_b64_tr_b16 v[52:53], v207 offset:39936
	v_mfma_f32_32x32x16_f16 v[82:97], v[114:117], v[134:137], v[82:97]
	v_add_f32_e32 v58, v64, v78
	v_add_f32_e32 v60, v65, v58
	v_cvt_pk_f16_f32 v132, v62, v63
	v_cvt_pk_f16_f32 v133, v64, v65
	s_add_i32 s26, s42, s36
	s_mov_b32 m0, s26
	s_nop 0
	global_load_lds_dwordx4 v221, s[50:51]
	s_add_i32 s26, s39, s35
	s_mov_b32 m0, s26
	s_nop 0
	global_load_lds_dwordx4 v222, s[52:53]
	v_max_f32_e32 v58, v98, v99
	v_max3_f32 v59, v100, v101, v83
	v_max3_f32 v58, v58, v82, v84
	v_max3_f32 v58, v58, v85, v102
	v_max3_f32 v59, v59, v104, v105
	v_max3_f32 v58, v58, v103, v86
	v_max3_f32 v59, v59, v88, v89
	v_max3_f32 v58, v58, v87, v106
	v_max3_f32 v59, v59, v108, v109
	v_max3_f32 v58, v58, v107, v90
	v_max3_f32 v59, v59, v92, v93
	v_max3_f32 v58, v58, v91, v110
	v_max3_f32 v59, v59, v112, v113
	v_max3_f32 v58, v58, v111, v94
	v_max3_f32 v59, v59, v96, v97
	v_max3_f32 v58, v58, v95, v59
	v_add_f32_e32 v198, v183, v60
	v_cmp_lt_f32_e32 vcc, s41, v58
	s_cmp_lg_u64 vcc, 0
	s_cselect_b64 s[26:27], -1, 0
	s_cbranch_vccnz .Lu2_9

.Lu2_4:
	s_add_i32 s26, s39, 0x2000
	s_cmpk_lg_i32 s39, 0x4000
	s_cselect_b32 s43, s26, 0
	ds_read_b64_tr_b16 v[126:127], v206 offset:40960
	ds_read_b64_tr_b16 v[128:129], v206 offset:41984
	s_waitcnt lgkmcnt(9)
	v_mfma_f32_32x32x16_f16 v[66:81], v[58:61], v[154:157], v[34:49]
	v_add_f32_e32 v50, v98, v99
	v_add_f32_e32 v50, v100, v50
	v_add_f32_e32 v50, v101, v50
	v_add_f32_e32 v50, v102, v50
	v_add_f32_e32 v50, v103, v50
	v_cvt_pk_f16_f32 v158, v98, v99
	v_cvt_pk_f16_f32 v159, v100, v101
	ds_read_b64_tr_b16 v[122:123], v207 offset:40960
	ds_read_b64_tr_b16 v[124:125], v207 offset:41984
	v_add_f32_e32 v50, v104, v50
	v_add_f32_e32 v50, v105, v50
	v_add_f32_e32 v50, v106, v50
	v_add_f32_e32 v98, v107, v50
	s_waitcnt lgkmcnt(10)
	v_mfma_f32_32x32x16_f16 v[50:65], v[114:117], v[154:157], v[34:49]
	v_cvt_pk_f16_f32 v160, v102, v103
	v_cvt_pk_f16_f32 v161, v104, v105
	ds_read_b64_tr_b16 v[118:119], v206 offset:43008
	ds_read_b64_tr_b16 v[120:121], v206 offset:44032
	s_waitcnt lgkmcnt(11)
	v_mfma_f32_32x32x16_f16 v[66:81], v[182:185], v[146:149], v[66:81]
	v_add_f32_e32 v98, v108, v98
	v_add_f32_e32 v98, v109, v98
	v_add_f32_e32 v98, v110, v98
	v_add_f32_e32 v98, v111, v98
	v_cvt_pk_f16_f32 v150, v106, v107
	v_cvt_pk_f16_f32 v151, v108, v109
	ds_read_b64_tr_b16 v[114:115], v207 offset:43008
	ds_read_b64_tr_b16 v[116:117], v207 offset:44032
	s_waitcnt lgkmcnt(12)
	v_mfma_f32_32x32x16_f16 v[50:65], v[174:177], v[146:149], v[50:65]
	v_add_f32_e32 v98, v112, v98
	v_add_f32_e32 v98, v113, v98
	v_add_f32_e32 v98, v82, v98
	v_add_f32_e32 v98, v83, v98
	v_cvt_pk_f16_f32 v152, v110, v111
	v_cvt_pk_f16_f32 v153, v112, v113
	ds_read_b64_tr_b16 v[106:107], v206 offset:45056
	ds_read_b64_tr_b16 v[108:109], v206 offset:46080
	s_waitcnt lgkmcnt(13)
	v_mfma_f32_32x32x16_f16 v[66:81], v[178:181], v[138:141], v[66:81]
	v_add_f32_e32 v98, v84, v98
	v_add_f32_e32 v98, v85, v98
	v_add_f32_e32 v98, v86, v98
	v_add_f32_e32 v98, v87, v98
	v_cvt_pk_f16_f32 v142, v82, v83
	v_cvt_pk_f16_f32 v143, v84, v85
	ds_read_b64_tr_b16 v[102:103], v207 offset:45056
	ds_read_b64_tr_b16 v[104:105], v207 offset:46080
	s_waitcnt lgkmcnt(14)
	v_mfma_f32_32x32x16_f16 v[50:65], v[166:169], v[138:141], v[50:65]
	v_add_f32_e32 v82, v88, v98
	v_add_f32_e32 v82, v89, v82
	v_add_f32_e32 v82, v90, v82
	v_add_f32_e32 v82, v91, v82
	v_cvt_pk_f16_f32 v144, v86, v87
	v_cvt_pk_f16_f32 v145, v88, v89
	ds_read_b64_tr_b16 v[98:99], v206 offset:47104
	ds_read_b64_tr_b16 v[100:101], v206 offset:48128
	s_waitcnt lgkmcnt(14)
	v_mfma_f32_32x32x16_f16 v[66:81], v[170:173], v[134:137], v[66:81]
	v_add_f32_e32 v82, v92, v82
	v_add_f32_e32 v82, v93, v82
	v_add_f32_e32 v82, v94, v82
	v_add_f32_e32 v82, v95, v82
	v_cvt_pk_f16_f32 v130, v90, v91
	v_cvt_pk_f16_f32 v131, v92, v93
	ds_read_b64_tr_b16 v[86:87], v207 offset:47104
	ds_read_b64_tr_b16 v[88:89], v207 offset:48128
	v_mfma_f32_32x32x16_f16 v[50:65], v[162:165], v[134:137], v[50:65]
	v_add_f32_e32 v82, v96, v82
	v_add_f32_e32 v84, v97, v82
	v_cvt_pk_f16_f32 v132, v94, v95
	v_cvt_pk_f16_f32 v133, v96, v97
	s_add_u32 s54, s50, 0x2000
	s_addc_u32 s55, s51, 0
	s_add_i32 s26, s39, s36
	s_mov_b32 m0, s26
	s_nop 0
	global_load_lds_dwordx4 v221, s[54:55]
	v_max_f32_e32 v82, v66, v67
	s_nop 1
	v_max3_f32 v83, v68, v69, v51
	v_max3_f32 v82, v82, v50, v52
	v_max3_f32 v82, v82, v53, v70
	v_max3_f32 v83, v83, v72, v73
	v_max3_f32 v82, v82, v71, v54
	v_max3_f32 v83, v83, v56, v57
	v_max3_f32 v82, v82, v55, v74
	v_max3_f32 v83, v83, v76, v77
	v_max3_f32 v82, v82, v75, v58
	v_max3_f32 v83, v83, v60, v61
	v_max3_f32 v82, v82, v59, v78
	v_max3_f32 v83, v83, v80, v81
	v_max3_f32 v82, v82, v79, v62
	v_max3_f32 v83, v83, v64, v65
	v_max3_f32 v82, v82, v63, v83
	v_add_f32_e32 v183, v198, v84
	s_add_u32 s54, s52, 0x2000
	s_addc_u32 s55, s53, 0
	s_add_i32 s26, s43, s35
	s_mov_b32 m0, s26
	s_nop 0
	global_load_lds_dwordx4 v222, s[54:55]
	v_cmp_lt_f32_e32 vcc, s41, v82
	s_cmp_lg_u64 vcc, 0
	s_cselect_b64 s[26:27], -1, 0
	s_cbranch_vccnz .Lu2_12

.Lu0_9:
	v_mov_b32_e32 v59, v58
	s_nop 1
	v_permlane32_swap_b32_e32 v58, v59
	v_max_f32_e32 v58, v58, v59
	v_max_f32_e32 v34, v58, v58
	v_max_f32_e32 v58, 0, v34
	v_exp_f32_e64 v59, -v58
	v_add_f32_e32 v205, v205, v58
	v_xor_b32_e32 v34, 0x80000000, v205
	v_mov_b32_e32 v35, v34
	v_mov_b32_e32 v36, v34
	v_mov_b32_e32 v37, v34
	v_mov_b32_e32 v38, v34
	v_mov_b32_e32 v39, v34
	v_mov_b32_e32 v40, v34
	v_mov_b32_e32 v41, v34
	v_mov_b32_e32 v42, v34
	v_mov_b32_e32 v43, v34
	v_mov_b32_e32 v44, v34
	v_mov_b32_e32 v45, v34
	v_mov_b32_e32 v46, v34
	v_mov_b32_e32 v47, v34
	v_mov_b32_e32 v48, v34
	v_mov_b32_e32 v49, v34
	s_and_saveexec_b64 s[28:29], s[0:1]
	ds_write_b32 v204, v59 offset:49152
	s_or_b64 exec, exec, s[28:29]
	v_sub_f32_e32 v113, v113, v58
	v_sub_f32_e32 v112, v112, v58
	v_sub_f32_e32 v111, v111, v58
	v_sub_f32_e32 v110, v110, v58
	v_sub_f32_e32 v109, v109, v58
	v_sub_f32_e32 v108, v108, v58
	v_sub_f32_e32 v107, v107, v58
	v_sub_f32_e32 v106, v106, v58
	v_sub_f32_e32 v105, v105, v58
	v_sub_f32_e32 v104, v104, v58
	v_sub_f32_e32 v103, v103, v58
	v_sub_f32_e32 v102, v102, v58
	v_sub_f32_e32 v101, v101, v58
	v_sub_f32_e32 v100, v100, v58
	v_sub_f32_e32 v99, v99, v58
	v_sub_f32_e32 v98, v98, v58
	v_sub_f32_e32 v97, v97, v58
	v_sub_f32_e32 v96, v96, v58
	v_sub_f32_e32 v95, v95, v58
	v_sub_f32_e32 v94, v94, v58
	v_sub_f32_e32 v93, v93, v58
	v_sub_f32_e32 v92, v92, v58
	v_sub_f32_e32 v91, v91, v58
	v_sub_f32_e32 v90, v90, v58
	v_sub_f32_e32 v89, v89, v58
	v_sub_f32_e32 v88, v88, v58
	v_sub_f32_e32 v87, v87, v58
	v_sub_f32_e32 v86, v86, v58
	v_sub_f32_e32 v85, v85, v58
	v_sub_f32_e32 v84, v84, v58
	v_sub_f32_e32 v83, v83, v58
	v_sub_f32_e32 v82, v82, v58
	v_mul_f32_e32 v198, v198, v59
	s_branch .Lu0_2
.Lu0_12:
	v_mov_b32_e32 v83, v82
	s_nop 1
	v_permlane32_swap_b32_e32 v82, v83
	v_max_f32_e32 v82, v82, v83
	v_max_f32_e32 v34, v82, v82
	v_max_f32_e32 v82, 0, v34
	v_exp_f32_e64 v83, -v82
	v_add_f32_e32 v205, v205, v82
	v_xor_b32_e32 v34, 0x80000000, v205
	v_mov_b32_e32 v35, v34
	v_mov_b32_e32 v36, v34
	v_mov_b32_e32 v37, v34
	v_mov_b32_e32 v38, v34
	v_mov_b32_e32 v39, v34
	v_mov_b32_e32 v40, v34
	v_mov_b32_e32 v41, v34
	v_mov_b32_e32 v42, v34
	v_mov_b32_e32 v43, v34
	v_mov_b32_e32 v44, v34
	v_mov_b32_e32 v45, v34
	v_mov_b32_e32 v46, v34
	v_mov_b32_e32 v47, v34
	v_mov_b32_e32 v48, v34
	v_mov_b32_e32 v49, v34
	s_and_saveexec_b64 s[28:29], s[0:1]
	ds_write_b32 v204, v83 offset:49152
	s_or_b64 exec, exec, s[28:29]
	v_sub_f32_e32 v81, v81, v82
	v_sub_f32_e32 v80, v80, v82
	v_sub_f32_e32 v79, v79, v82
	v_sub_f32_e32 v78, v78, v82
	v_sub_f32_e32 v77, v77, v82
	v_sub_f32_e32 v76, v76, v82
	v_sub_f32_e32 v75, v75, v82
	v_sub_f32_e32 v74, v74, v82
	v_sub_f32_e32 v73, v73, v82
	v_sub_f32_e32 v72, v72, v82
	v_sub_f32_e32 v71, v71, v82
	v_sub_f32_e32 v70, v70, v82
	v_sub_f32_e32 v69, v69, v82
	v_sub_f32_e32 v68, v68, v82
	v_sub_f32_e32 v67, v67, v82
	v_sub_f32_e32 v66, v66, v82
	v_sub_f32_e32 v65, v65, v82
	v_sub_f32_e32 v64, v64, v82
	v_sub_f32_e32 v63, v63, v82
	v_sub_f32_e32 v62, v62, v82
	v_sub_f32_e32 v61, v61, v82
	v_sub_f32_e32 v60, v60, v82
	v_sub_f32_e32 v59, v59, v82
	v_sub_f32_e32 v58, v58, v82
	v_sub_f32_e32 v57, v57, v82
	v_sub_f32_e32 v56, v56, v82
	v_sub_f32_e32 v55, v55, v82
	v_sub_f32_e32 v54, v54, v82
	v_sub_f32_e32 v53, v53, v82
	v_sub_f32_e32 v52, v52, v82
	v_sub_f32_e32 v51, v51, v82
	v_sub_f32_e32 v50, v50, v82
	v_mul_f32_e32 v183, v183, v83
	s_branch .Lu0_5
